# speedup vs baseline: 1.0471x; 1.0471x over previous
_Z14seg_sum_kernelPKfS0_S0_PDv8_DF16bS2_Pf:
	s_and_b32 s3, s2, 7
	s_load_dwordx4 s[12:15], s[0:1], 0x0
	s_lshl_b32 s3, s3, 3
	s_bfe_u32 s4, s2, 0x30005
	s_or_b32 s3, s3, s4
	v_readfirstlane_b32 s5, v0
	s_ashr_i32 s4, s3, 2
	s_lshr_b32 s11, s5, 6
	s_mul_hi_u32 s5, s5, 0xaaaaaaab
	s_lshr_b32 s23, s5, 7
	s_ashr_i32 s5, s4, 31
	s_and_b32 s22, s3, 3
	s_and_b32 s37, s2, 3
	s_lshl_b64 s[6:7], s[4:5], 19
	s_waitcnt lgkmcnt(0)
	s_add_u32 s5, s14, s6
	s_addc_u32 s6, s15, s7
	s_lshl_b32 s14, s22, 10
	s_lshl_b32 s8, s22, 12
	s_add_u32 s8, s5, s8
	v_lshlrev_b32_e32 v2, 6, v0
	v_add_u32_e32 v122, 0x300, v0
	s_addc_u32 s9, s6, 0
	v_lshlrev_b32_e32 v1, 4, v0
	v_and_b32_e32 v2, 0xc000, v2
	v_mov_b32_e32 v3, 0
	v_lshlrev_b32_e32 v6, 6, v122
	v_lshl_add_u64 v[4:5], s[8:9], 0, v[2:3]
	v_and_b32_e32 v2, 0xff0, v1
	v_lshlrev_b32_e32 v1, 4, v122
	v_and_b32_e32 v6, 0x1c000, v6
	v_mov_b32_e32 v7, v3
	v_lshl_add_u64 v[4:5], v[4:5], 0, v[2:3]
	v_lshl_add_u64 v[6:7], s[8:9], 0, v[6:7]
	v_and_b32_e32 v8, 0xff0, v1
	v_mov_b32_e32 v9, v3
	v_add_u32_e32 v123, 0x600, v0
	v_lshl_add_u64 v[6:7], v[6:7], 0, v[8:9]
	global_load_dwordx4 v[82:85], v[4:5], off nt
	global_load_dwordx4 v[78:81], v[6:7], off nt
	v_lshlrev_b32_e32 v4, 6, v123
	v_lshlrev_b32_e32 v1, 4, v123
	v_and_b32_e32 v4, 0x3c000, v4
	v_mov_b32_e32 v5, v3
	v_lshl_add_u64 v[4:5], s[8:9], 0, v[4:5]
	v_and_b32_e32 v6, 0xff0, v1
	v_mov_b32_e32 v7, v3
	v_add_u32_e32 v124, 0x900, v0
	v_lshl_add_u64 v[4:5], v[4:5], 0, v[6:7]
	v_lshlrev_b32_e32 v6, 6, v124
	v_lshlrev_b32_e32 v1, 4, v124
	v_and_b32_e32 v6, 0x3c000, v6
	v_lshl_add_u64 v[6:7], s[8:9], 0, v[6:7]
	v_and_b32_e32 v8, 0xff0, v1
	v_or_b32_e32 v125, 0xc00, v0
	v_lshl_add_u64 v[6:7], v[6:7], 0, v[8:9]
	v_lshlrev_b32_e32 v1, 6, v125
	v_add_u32_e32 v130, 0xf00, v0
	global_load_dwordx4 v[90:93], v[4:5], off nt
	global_load_dwordx4 v[86:89], v[6:7], off nt
	v_and_b32_e32 v4, 0x3c000, v1
	v_mov_b32_e32 v5, v3
	v_lshlrev_b32_e32 v6, 6, v130
	v_lshl_add_u64 v[4:5], s[8:9], 0, v[4:5]
	v_lshlrev_b32_e32 v1, 4, v130
	v_and_b32_e32 v6, 0x7c000, v6
	v_mov_b32_e32 v7, v3
	v_lshl_add_u64 v[4:5], v[4:5], 0, v[2:3]
	v_lshl_add_u64 v[6:7], s[8:9], 0, v[6:7]
	v_and_b32_e32 v8, 0xff0, v1
	v_add_u32_e32 v131, 0x1200, v0
	v_lshl_add_u64 v[6:7], v[6:7], 0, v[8:9]
	global_load_dwordx4 v[98:101], v[4:5], off nt
	global_load_dwordx4 v[94:97], v[6:7], off nt
	v_lshlrev_b32_e32 v4, 6, v131
	v_lshlrev_b32_e32 v1, 4, v131
	v_and_b32_e32 v4, 0x5c000, v4
	v_mov_b32_e32 v5, v3
	v_lshl_add_u64 v[4:5], s[8:9], 0, v[4:5]
	v_and_b32_e32 v6, 0xff0, v1
	v_mov_b32_e32 v7, v3
	v_add_u32_e32 v134, 0x1500, v0
	v_lshl_add_u64 v[4:5], v[4:5], 0, v[6:7]
	v_lshlrev_b32_e32 v6, 6, v134
	v_lshlrev_b32_e32 v1, 4, v134
	v_and_b32_e32 v6, 0x7c000, v6
	v_or_b32_e32 v135, 0x1800, v0
	v_lshl_add_u64 v[6:7], s[8:9], 0, v[6:7]
	v_and_b32_e32 v8, 0xff0, v1
	v_lshlrev_b32_e32 v1, 6, v135
	v_lshl_add_u64 v[6:7], v[6:7], 0, v[8:9]
	global_load_dwordx4 v[106:109], v[4:5], off nt
	global_load_dwordx4 v[102:105], v[6:7], off nt
	v_and_b32_e32 v4, 0x6c000, v1
	v_mov_b32_e32 v5, v3
	v_lshl_add_u64 v[4:5], s[8:9], 0, v[4:5]
	v_add_u32_e32 v136, 0x1b00, v0
	v_lshl_add_u64 v[4:5], v[4:5], 0, v[2:3]
	v_lshlrev_b32_e32 v2, 6, v136
	v_lshlrev_b32_e32 v1, 4, v136
	v_and_b32_e32 v2, 0x7c000, v2
	v_lshl_add_u64 v[6:7], s[8:9], 0, v[2:3]
	v_and_b32_e32 v2, 0xff0, v1
	v_add_u32_e32 v137, 0x1e00, v0
	v_lshl_add_u64 v[6:7], v[6:7], 0, v[2:3]
	v_min_u32_e32 v1, 0x1fff, v137
	global_load_dwordx4 v[118:121], v[4:5], off nt
	global_load_dwordx4 v[110:113], v[6:7], off nt
	v_lshlrev_b32_e32 v6, 4, v1
	v_lshlrev_b32_e32 v1, 6, v1
	v_and_b32_e32 v2, 0x7c000, v1
	v_bfe_u32 v127, v0, 4, 2
	s_lshl_b32 s4, s4, 12
	v_lshl_add_u64 v[4:5], s[8:9], 0, v[2:3]
	v_and_b32_e32 v2, 0xff0, v6
	v_lshlrev_b32_e32 v133, 3, v127
	s_or_b32 s4, s14, s4
	v_lshl_add_u64 v[4:5], v[4:5], 0, v[2:3]
	s_lshl_b32 s26, s23, 8
	v_or_b32_e32 v2, s4, v133
	s_movk_i32 s10, 0xc00
	global_load_dwordx4 v[114:117], v[4:5], off nt
	s_mul_hi_u32 s6, s11, 0x55555556
	v_add_u32_e32 v28, s26, v2
	v_mov_b64_e32 v[4:5], s[12:13]
	s_mov_b32 s7, 0
	s_bfe_u32 s24, s2, 0x20003
	s_mul_i32 s6, s6, 3
	v_mad_i64_i32 v[4:5], s[8:9], v28, s10, v[4:5]
	s_sub_i32 s25, s11, s6
	s_mul_i32 s8, s24, 0x300
	s_mov_b32 s9, s7
	v_and_b32_e32 v1, 15, v0
	v_lshl_add_u64 v[4:5], v[4:5], 0, s[8:9]
	s_lshl_b32 s8, s25, 8
	v_lshl_add_u64 v[4:5], v[4:5], 0, s[8:9]
	v_lshlrev_b32_e32 v2, 4, v1
	v_lshl_add_u64 v[4:5], v[4:5], 0, v[2:3]
	s_movk_i32 s4, 0x1000
	v_add_co_u32_e32 v6, vcc, s4, v4
	s_movk_i32 s4, 0x2000
	s_nop 0
	v_addc_co_u32_e32 v7, vcc, 0, v5, vcc
	v_add_co_u32_e32 v8, vcc, s4, v4
	s_movk_i32 s4, 0x3000
	s_nop 0
	v_addc_co_u32_e32 v9, vcc, 0, v5, vcc
	global_load_dwordx4 v[18:21], v[4:5], off nt
	global_load_dwordx4 v[30:33], v[4:5], off offset:3072 nt
	global_load_dwordx4 v[46:49], v[6:7], off offset:2048 nt
	global_load_dwordx4 v[50:53], v[8:9], off offset:1024 nt
	v_add_co_u32_e32 v6, vcc, s4, v4
	s_movk_i32 s4, 0x4000
	s_nop 0
	v_addc_co_u32_e32 v7, vcc, 0, v5, vcc
	global_load_dwordx4 v[62:65], v[6:7], off nt
	global_load_dwordx4 v[66:69], v[6:7], off offset:3072 nt
	v_add_co_u32_e32 v6, vcc, s4, v4
	s_movk_i32 s4, 0x5000
	s_nop 0
	v_addc_co_u32_e32 v7, vcc, 0, v5, vcc
	v_add_co_u32_e32 v8, vcc, s4, v4
	s_mov_b32 s4, 0x18000
	s_nop 0
	v_addc_co_u32_e32 v9, vcc, 0, v5, vcc
	v_add_co_u32_e32 v10, vcc, s4, v4
	s_mov_b32 s4, 0x19000
	s_nop 0
	v_addc_co_u32_e32 v11, vcc, 0, v5, vcc
	v_add_co_u32_e32 v14, vcc, s4, v4
	s_mov_b32 s4, 0x1a000
	s_nop 0
	v_addc_co_u32_e32 v15, vcc, 0, v5, vcc
	v_add_co_u32_e32 v22, vcc, s4, v4
	s_mov_b32 s4, 0x1b000
	s_nop 0
	v_addc_co_u32_e32 v23, vcc, 0, v5, vcc
	v_add_co_u32_e32 v26, vcc, s4, v4
	s_mov_b32 s5, 0x1c000
	s_nop 0
	v_addc_co_u32_e32 v27, vcc, 0, v5, vcc
	global_load_dwordx4 v[70:73], v[6:7], off offset:2048 nt
	global_load_dwordx4 v[74:77], v[8:9], off offset:1024 nt
	s_nop 0
	global_load_dwordx4 v[6:9], v[10:11], off nt
	s_nop 0
	global_load_dwordx4 v[10:13], v[10:11], off offset:3072 nt
	s_nop 0
	global_load_dwordx4 v[14:17], v[14:15], off offset:2048 nt
	s_nop 0
	global_load_dwordx4 v[22:25], v[22:23], off offset:1024 nt
	s_nop 0
	global_load_dwordx4 v[38:41], v[26:27], off nt
	global_load_dwordx4 v[42:45], v[26:27], off offset:3072 nt
	v_add_co_u32_e32 v26, vcc, s5, v4
	s_mov_b32 s4, 0x1d000
	s_nop 0
	v_addc_co_u32_e32 v27, vcc, 0, v5, vcc
	v_add_co_u32_e32 v4, vcc, s4, v4
	v_lshrrev_b32_e32 v126, 3, v0
	s_nop 0
	v_addc_co_u32_e32 v5, vcc, 0, v5, vcc
	global_load_dwordx4 v[54:57], v[26:27], off offset:2048 nt
	global_load_dwordx4 v[58:61], v[4:5], off offset:1024 nt
	v_mad_i64_i32 v[4:5], s[4:5], v28, s10, 0
	s_lshl_b32 s4, s2, 1
	s_nop 0
	v_bfi_b32 v132, -8, s4, v0
	v_mad_u64_u32 v[128:129], s[4:5], s37, 24, v[126:127]
	s_movk_i32 s4, 0xc0
	s_lshl_b32 s6, s25, 6
	v_cmp_gt_u32_e64 s[4:5], s4, v0
	v_mov_b32_e32 v26, v3
	v_mov_b32_e32 v27, v3
	v_mov_b32_e32 v28, v3
	v_mov_b32_e32 v29, v3
	v_mov_b32_e32 v34, v3
	v_mov_b32_e32 v35, v3
	v_mov_b32_e32 v36, v3
	v_mov_b32_e32 v37, v3
	s_and_saveexec_b64 s[8:9], s[4:5]
	s_cbranch_execz .LBB0_2
	s_load_dwordx2 s[14:15], s[0:1], 0x10
	v_lshlrev_b32_e32 v26, 5, v128
	v_mov_b32_e32 v27, 0
	s_waitcnt lgkmcnt(0)
	v_mov_b64_e32 v[28:29], s[14:15]
	v_mad_i64_i32 v[28:29], s[10:11], v132, s10, v[28:29]
	v_lshl_add_u64 v[34:35], v[28:29], 0, v[26:27]
	global_load_dwordx4 v[26:29], v[34:35], off offset:16 nt
	s_nop 0
	global_load_dwordx4 v[34:37], v[34:35], off nt

.Lseg_rd:
	v_add_u32_e32 v27, 0x10000, v26
	s_lshl_b32 s0, s0, 2
	ds_read_b128 v[10:13], v27 offset:512
	ds_read_b128 v[14:17], v27 offset:528
	ds_read_b128 v[18:21], v27 offset:25600
	ds_read_b128 v[22:25], v27 offset:25616
	ds_read_b128 v[34:37], v27 offset:50688
	ds_read_b128 v[38:41], v27 offset:50704
	s_or_b32 s0, s0, s24
	s_mul_hi_i32 s1, s0, 0x3000
	s_mulk_i32 s0, 0x3000
	s_add_u32 s0, s8, s0
	s_addc_u32 s1, s9, s1
	s_waitcnt lgkmcnt(0)
	s_barrier
	ds_read_b128 v[2:5], v26
	ds_read_b128 v[6:9], v26 offset:16
	v_mov_b32_e32 v1, 0
	s_cmp_eq_u32 s24, 0
	s_waitcnt lgkmcnt(0)
	v_pk_add_f32 v[8:9], v[8:9], 0 op_sel_hi:[1,0]
	v_pk_add_f32 v[4:5], v[4:5], 0 op_sel_hi:[1,0]
	v_pk_add_f32 v[6:7], v[6:7], 0 op_sel_hi:[1,0]
	v_pk_add_f32 v[2:3], v[2:3], 0 op_sel_hi:[1,0]
	v_pk_add_f32 v[4:5], v[4:5], v[12:13]
	v_pk_add_f32 v[8:9], v[8:9], v[16:17]
	v_pk_add_f32 v[2:3], v[2:3], v[10:11]
	v_pk_add_f32 v[6:7], v[6:7], v[14:15]
	v_pk_add_f32 v[8:9], v[8:9], v[24:25]
	v_pk_add_f32 v[4:5], v[4:5], v[20:21]
	v_pk_add_f32 v[6:7], v[6:7], v[22:23]
	v_pk_add_f32 v[2:3], v[2:3], v[18:19]
	v_pk_add_f32 v[10:11], v[4:5], v[36:37]
	v_pk_add_f32 v[4:5], v[8:9], v[40:41]
	v_pk_add_f32 v[8:9], v[2:3], v[34:35]
	v_pk_add_f32 v[6:7], v[6:7], v[38:39]
	v_lshl_add_u64 v[12:13], v[0:1], 4, s[0:1]
	s_cselect_b64 s[0:1], -1, 0
	v_cmp_gt_u32_e32 vcc, 32, v0
	v_cvt_pk_bf16_f32 v5, v4, v5
	v_cvt_pk_bf16_f32 v3, v10, v11
	v_cvt_pk_bf16_f32 v4, v6, v7
	v_cvt_pk_bf16_f32 v2, v8, v9
	s_and_b64 s[0:1], s[0:1], vcc
	global_store_dwordx4 v[12:13], v[2:5], off
	s_and_saveexec_b64 s[4:5], s[0:1]
	s_cbranch_execz .LBB0_20
	v_mov_b32_e32 v1, 0x22800
	v_lshl_add_u32 v1, v0, 2, v1
	ds_read2_b32 v[2:3], v1 offset1:32
	ds_read2_b32 v[4:5], v1 offset0:64 offset1:96
	v_lshl_or_b32 v0, s3, 5, v0
	v_ashrrev_i32_e32 v1, 31, v0
	v_lshl_add_u64 v[0:1], v[0:1], 2, s[10:11]
	s_waitcnt lgkmcnt(1)
	v_add_f32_e32 v2, 0, v2
	v_add_f32_e32 v2, v2, v3
	s_waitcnt lgkmcnt(0)
	v_add_f32_e32 v2, v2, v4
	v_add_f32_e32 v2, v2, v5
	global_store_dword v[0:1], v2, off
